# v068
# speedup vs baseline: 1.1524x; 1.0050x over previous
.LBB2_23:
	s_add_i32 s4, s35, 0x800
	s_add_i32 s6, s93, 0x80
	s_add_u32 s4, s8, s4
	s_addc_u32 s5, s9, 0
	s_add_u32 s6, s8, s6
	s_addc_u32 s7, s9, 0
	v_and_b32_e32 v1, 15, v0
	v_lshlrev_b32_e32 v2, 2, v0
	s_waitcnt vmcnt(4)
	s_barrier
	s_add_i32 s60, s52, 0x18000
	s_mov_b32 m0, s60
	s_nop 0
	global_load_lds_dwordx4 v215, s[6:7]
	v_lshl_or_b32 v227, s3, 6, v1
	v_lshl_or_b32 v1, v1, 6, v194
	s_lshl_b32 s3, s3, 13
	v_and_b32_e32 v2, 32, v2
	s_add_i32 s61, s52, 0x1a000
	s_mov_b32 m0, s61
	s_nop 0
	global_load_lds_dwordx4 v223, s[6:7]
	v_bitop3_b32 v1, v1, s3, v2 bitop3:0xde
	v_lshlrev_b32_e32 v0, 6, v0
	s_movk_i32 s3, 0x3c0
	s_lshl_b32 s0, s0, 12
	s_add_i32 s63, s52, 0x8000
	s_mov_b32 m0, s63
	s_nop 0
	global_load_lds_dwordx4 v213, s[4:5]
	s_add_i32 s64, s52, 0xa000
	v_and_or_b32 v0, v0, s3, v194
	s_mov_b32 m0, s64
	s_nop 0
	global_load_lds_dwordx4 v221, s[4:5]
	s_add_u32 s4, s6, 0x40000
	v_bitop3_b32 v0, s0, v0, v2 bitop3:0xf6
	s_addc_u32 s5, s7, 0
	s_lshl_b32 s0, s2, 1
	s_and_b32 s0, s0, 14
	s_ashr_i32 s3, s2, 5
	s_mul_i32 s0, s13, s0
	s_add_i32 s12, s0, s3
	s_ashr_i32 s0, s12, 1
	s_and_b32 s0, s0, -8
	s_sub_i32 s0, 24, s0
	s_lshr_b32 s14, s1, s0
	s_bfe_u32 s69, s14, 0x50003
	v_sub_co_u32_e64 v2, s[0:1], s69, 1
	s_bfe_u32 s67, s2, 0x20003
	v_readfirstlane_b32 s2, v2
	s_and_b32 s68, s14, 7
	s_lshl_b32 s2, s2, 21
	s_lshl_b32 s15, s68, 22
	s_and_b32 s3, s2, 0x200000
	s_or_b32 s3, s3, s15
	s_add_i32 s65, s52, 0x1c000
	s_add_i32 s66, s52, 0x1e000
	s_lshl_b32 s17, s67, 18
	s_bitset1_b32 s3, 27
	s_add_i32 s2, s2, 0x9c00000
	s_cmp_eq_u32 s68, 7
	s_cselect_b32 s2, s2, s3
	s_or_b32 s18, s17, s2
	s_add_u32 s2, s8, 0xd600000
	s_mov_b32 m0, s65
	s_nop 0
	global_load_lds_dwordx4 v215, s[4:5]
	s_addc_u32 s3, s9, 0
	s_add_i32 s70, s52, 0x20000
	s_add_i32 s72, s52, 0xc000
	s_mov_b32 m0, s66
	s_nop 0
	global_load_lds_dwordx4 v223, s[4:5]
	s_add_u32 s4, s8, 0xf830000
	s_addc_u32 s5, s9, 0
	s_add_u32 s6, s8, 0xf8a0000
	s_addc_u32 s7, s9, 0
	s_add_u32 s73, s8, 0xf8d0000
	s_addc_u32 s74, s9, 0
	s_add_i32 s75, s52, 0x22000
	s_add_i32 s76, s52, 0x24000
	s_add_i32 s77, s52, 0x26000
	s_add_i32 s78, s52, 0xe000
	s_lshl_b32 s10, s13, 3
	s_cmp_lt_i32 s16, s10
	s_cselect_b64 s[10:11], -1, 0
	s_and_b32 s79, s12, 15
	s_lshl_b32 s12, s68, 23
	s_lshl_b32 s13, s79, 19
	s_or_b32 s16, s12, s13
	s_lshl_b32 s12, s14, 18
	s_and_b32 s12, s12, 0x200000
	s_or_b32 s13, s15, s12
	s_add_i32 s19, s13, 0x7c00000
	s_xor_b32 s14, s12, 0x8200000
	s_and_b64 s[12:13], s[0:1], exec
	s_cselect_b32 s20, 0xd400000, s14
	s_cmp_eq_u32 s68, 0
	s_cselect_b64 s[12:13], -1, 0
	s_and_b64 s[14:15], s[12:13], exec
	s_cselect_b32 s14, 0x400, 0
	s_cselect_b32 s15, s20, s19
	s_or_b64 s[0:1], s[12:13], s[0:1]
	s_or_b32 s80, s16, s14
	s_or_b32 s12, s69, s68
	s_or_b32 s81, s15, s17
	s_addk_i32 s18, 0xc000
	s_and_b64 s[0:1], s[0:1], exec
	v_mov_b32_e32 v197, v195
	s_cselect_b32 s0, 8, 16
	s_cselect_b32 s82, s81, s18
	s_cmp_lg_u32 s12, 0
	v_add_u32_e32 v0, 0, v0
	s_mov_b32 s62, 0x8000
	s_mov_b32 s71, 0xc000
	v_lshl_add_u64 v[198:199], s[2:3], 0, v[196:197]
	v_or_b32_e32 v197, 0x4000, v196
	v_or_b32_e32 v228, 0x6000, v196
	v_or_b32_e32 v229, s50, v225
	s_cselect_b32 s83, s0, 2
	s_xor_b64 s[10:11], s[10:11], -1
	v_add_u32_e32 v230, 0x10000, v0
	v_lshrrev_b32_e32 v250, 6, v227
	v_lshlrev_b32_e32 v250, 13, v250
	v_lshl_or_b32 v250, v194, 4, v250
	v_and_b32_e32 v251, 15, v227
	v_lshl_or_b32 v231, v251, 4, v250
	v_mov_b32_e32 v232, 0x75757575
	v_mov_b32_e32 v233, 0x77777777
	v_add_u32_e32 v234, 0x14000, v0
	v_add_u32_e32 v235, 0x18000, v0
	v_add_u32_e32 v236, 0x1c000, v0
	s_mov_b64 s[12:13], 0x4000
	s_mov_b64 s[14:15], 0x8000
	s_mov_b64 s[16:17], 0xc000
	s_mov_b64 s[18:19], 0x2000
	s_mov_b64 s[20:21], 0x6000
	s_mov_b64 s[22:23], 0xa000
	s_mov_b64 s[24:25], 0xe000
	v_add_u32_e32 v246, 0x20000, v213
	v_add_u32_e32 v247, 0x20000, v221
	v_add_u32_e32 v248, 0x40000, v215
	v_add_u32_e32 v249, 0x40000, v223
	s_waitcnt vmcnt(6)
	s_barrier
	s_branch .LBB2_25
